# attention epilogue: 16 row sum-of-squares reductions done stage-by-stage in place (no DPP hazard nops) with bpermutes in two groups instead of 16 serial round trips; on top of v6
# speedup vs baseline: 1.0020x; 1.0020x over previous
.LBB0_1136:
	s_or_b64 exec, exec, s[0:1]
	s_movk_i32 s0, 0x100
	v_cmp_gt_u32_e32 vcc, s0, v165
	s_waitcnt lgkmcnt(0)
	s_barrier
	s_and_saveexec_b64 s[12:13], vcc
	s_cbranch_execz .LBB0_1116
	v_lshlrev_b32_e32 v107, 8, v165
	v_lshl_add_u32 v106, v200, 2, 0
	v_and_b32_e32 v66, 0xc000, v107
	v_add_u32_e32 v108, v106, v66
	ds_read2st64_b32 v[136:137], v108 offset1:1
	ds_read2st64_b32 v[138:139], v108 offset0:2 offset1:3
	ds_read2st64_b32 v[140:141], v108 offset0:4 offset1:5
	ds_read2st64_b32 v[142:143], v108 offset0:6 offset1:7
	ds_read2st64_b32 v[144:145], v108 offset0:8 offset1:9
	ds_read2st64_b32 v[146:147], v108 offset0:10 offset1:11
	ds_read2st64_b32 v[148:149], v108 offset0:14 offset1:15
	ds_read2st64_b32 v[150:151], v108 offset0:12 offset1:13
	ds_read2st64_b32 v[152:153], v108 offset0:18 offset1:19
	ds_read2st64_b32 v[154:155], v108 offset0:16 offset1:17
	v_lshlrev_b32_e32 v162, 2, v175
	s_lshl_b64 s[0:1], s[6:7], 11
	v_readlane_b32 s2, v251, 35
	s_add_u32 s0, s2, s0
	s_waitcnt lgkmcnt(9)
	v_fma_f32 v73, v50, v105, -v136
	v_fma_f32 v72, v51, v104, -v137
	v_readlane_b32 s2, v251, 37
	s_addc_u32 s1, s2, s1
	s_lshl_b32 s2, s39, 8
	s_add_u32 s6, s0, s2
	s_waitcnt lgkmcnt(8)
	v_fma_f32 v71, v52, v101, -v138
	v_fma_f32 v70, v53, v99, -v139
	s_addc_u32 s7, s1, 0
	v_mov_b32_e32 v165, v163
	s_movk_i32 s0, 0x1000
	s_waitcnt lgkmcnt(7)
	v_fma_f32 v69, v54, v95, -v140
	v_fma_f32 v67, v55, v102, -v141
	s_waitcnt lgkmcnt(6)
	v_fma_f32 v68, v56, v98, -v142
	v_fma_f32 v66, v57, v96, -v143
	s_waitcnt lgkmcnt(5)
	v_fma_f32 v57, v58, v103, -v144
	v_fma_f32 v56, v59, v100, -v145
	s_waitcnt lgkmcnt(4)
	v_fma_f32 v55, v60, v97, -v146
	v_fma_f32 v54, v61, v94, -v147
	s_waitcnt lgkmcnt(3)
	v_fma_f32 v52, v64, v91, -v148
	s_waitcnt lgkmcnt(2)
	v_fma_f32 v53, v62, v93, -v150
	v_fma_f32 v50, v65, v90, -v149
	v_fma_f32 v51, v63, v92, -v151
	s_waitcnt lgkmcnt(0)
	v_fma_f32 v35, v35, v104, -v155
	s_waitcnt lgkmcnt(1)
	v_fma_f32 v59, v36, v101, -v152
	v_fma_f32 v36, v37, v99, -v153
	v_fma_f32 v58, v34, v105, -v154
	ds_read2st64_b32 v[136:137], v108 offset0:26 offset1:27
	ds_read2st64_b32 v[138:139], v108 offset0:20 offset1:21
	ds_read2st64_b32 v[140:141], v108 offset0:22 offset1:23
	ds_read2st64_b32 v[142:143], v108 offset0:24 offset1:25
	ds_read2st64_b32 v[144:145], v108 offset0:28 offset1:29
	ds_read2st64_b32 v[146:147], v108 offset0:30 offset1:31
	ds_read2st64_b32 v[148:149], v108 offset0:32 offset1:33
	ds_read2st64_b32 v[150:151], v108 offset0:34 offset1:35
	ds_read2st64_b32 v[152:153], v108 offset0:36 offset1:37
	ds_read2st64_b32 v[154:155], v108 offset0:38 offset1:39
	ds_read2st64_b32 v[156:157], v108 offset0:40 offset1:41
	ds_read2st64_b32 v[158:159], v108 offset0:42 offset1:43
	ds_read2st64_b32 v[160:161], v108 offset0:46 offset1:47
	ds_read2st64_b32 v[226:227], v108 offset0:44 offset1:45
	v_mul_f32_e32 v86, v58, v58
	v_fmac_f32_e32 v86, v73, v73
	v_mul_f32_e32 v82, v35, v35
	s_waitcnt lgkmcnt(12)
	v_fma_f32 v37, v38, v95, -v138
	v_fma_f32 v34, v39, v102, -v139
	v_fmac_f32_e32 v82, v72, v72
	v_mul_f32_e32 v83, v59, v59
	v_fmac_f32_e32 v83, v71, v71
	v_mul_f32_e32 v78, v36, v36
	s_waitcnt lgkmcnt(11)
	v_fma_f32 v61, v40, v98, -v140
	v_fma_f32 v60, v41, v96, -v141
	s_waitcnt lgkmcnt(13)
	v_fma_f32 v40, v45, v94, -v137
	v_fmac_f32_e32 v78, v70, v70
	v_mul_f32_e32 v80, v37, v37
	v_fmac_f32_e32 v80, v69, v69
	s_waitcnt lgkmcnt(10)
	v_fma_f32 v41, v42, v103, -v142
	v_fma_f32 v38, v43, v100, -v143
	v_fma_f32 v43, v44, v97, -v136
	v_mul_f32_e32 v74, v34, v34
	v_fmac_f32_e32 v74, v67, v67
	v_mul_f32_e32 v89, v61, v61
	v_fmac_f32_e32 v89, v68, v68
	s_waitcnt lgkmcnt(9)
	v_fma_f32 v42, v46, v93, -v144
	v_fma_f32 v39, v47, v92, -v145
	v_mul_f32_e32 v87, v60, v60
	v_fmac_f32_e32 v87, v66, v66
	v_mul_f32_e32 v84, v41, v41
	v_fmac_f32_e32 v84, v57, v57
	s_waitcnt lgkmcnt(8)
	v_fma_f32 v45, v48, v91, -v146
	v_fma_f32 v44, v49, v90, -v147
	v_mul_f32_e32 v79, v38, v38
	v_fmac_f32_e32 v79, v56, v56
	v_mul_f32_e32 v81, v43, v43
	v_fmac_f32_e32 v81, v55, v55
	s_waitcnt lgkmcnt(7)
	v_fma_f32 v76, v18, v105, -v148
	v_fma_f32 v63, v19, v104, -v149
	v_fmac_f32_e32 v86, v76, v76
	v_fmac_f32_e32 v82, v63, v63
	v_mul_f32_e32 v75, v40, v40
	v_fmac_f32_e32 v75, v54, v54
	s_waitcnt lgkmcnt(6)
	v_fma_f32 v65, v20, v101, -v150
	v_fma_f32 v62, v21, v99, -v151
	v_fmac_f32_e32 v83, v65, v65
	v_fmac_f32_e32 v78, v62, v62
	v_mul_f32_e32 v77, v42, v42
	v_fmac_f32_e32 v77, v53, v53
	s_waitcnt lgkmcnt(5)
	v_fma_f32 v49, v22, v95, -v152
	v_fma_f32 v48, v23, v102, -v153
	v_fmac_f32_e32 v80, v49, v49
	v_fmac_f32_e32 v74, v48, v48
	v_mul_f32_e32 v64, v39, v39
	v_fmac_f32_e32 v64, v51, v51
	s_waitcnt lgkmcnt(4)
	v_fma_f32 v47, v24, v98, -v154
	v_fma_f32 v46, v25, v96, -v155
	v_fmac_f32_e32 v89, v47, v47
	v_fmac_f32_e32 v87, v46, v46
	v_mul_f32_e32 v88, v45, v45
	v_fmac_f32_e32 v88, v52, v52
	s_waitcnt lgkmcnt(3)
	v_fma_f32 v25, v26, v103, -v156
	v_fma_f32 v24, v27, v100, -v157
	v_fmac_f32_e32 v84, v25, v25
	v_fmac_f32_e32 v79, v24, v24
	v_mul_f32_e32 v85, v44, v44
	s_waitcnt lgkmcnt(2)
	v_fma_f32 v23, v28, v97, -v158
	v_fma_f32 v22, v29, v94, -v159
	v_fmac_f32_e32 v81, v23, v23
	v_fmac_f32_e32 v75, v22, v22
	v_fmac_f32_e32 v85, v50, v50
	s_waitcnt lgkmcnt(0)
	v_fma_f32 v21, v30, v93, -v226
	v_fma_f32 v20, v31, v92, -v227
	s_waitcnt lgkmcnt(1)
	v_fma_f32 v19, v32, v91, -v160
	v_fma_f32 v18, v33, v90, -v161
	ds_read2st64_b32 v[136:137], v108 offset0:48 offset1:49
	ds_read2st64_b32 v[138:139], v108 offset0:50 offset1:51
	ds_read2st64_b32 v[140:141], v108 offset0:52 offset1:53
	ds_read2st64_b32 v[142:143], v108 offset0:54 offset1:55
	ds_read2st64_b32 v[144:145], v108 offset0:56 offset1:57
	ds_read2st64_b32 v[146:147], v108 offset0:58 offset1:59
	ds_read2st64_b32 v[148:149], v108 offset0:60 offset1:61
	v_fmac_f32_e32 v77, v21, v21
	v_fmac_f32_e32 v64, v20, v20
	v_fmac_f32_e32 v88, v19, v19
	v_fmac_f32_e32 v85, v18, v18
	s_waitcnt lgkmcnt(6)
	v_fma_f32 v33, v2, v105, -v136
	v_fma_f32 v32, v3, v104, -v137
	v_fmac_f32_e32 v86, v33, v33
	v_fmac_f32_e32 v82, v32, v32
	s_waitcnt lgkmcnt(5)
	v_fma_f32 v31, v4, v101, -v138
	v_fma_f32 v30, v5, v99, -v139
	v_fmac_f32_e32 v83, v31, v31
	v_fmac_f32_e32 v78, v30, v30
	s_waitcnt lgkmcnt(4)
	v_fma_f32 v29, v6, v95, -v140
	v_fma_f32 v28, v7, v102, -v141
	v_fmac_f32_e32 v80, v29, v29
	v_fmac_f32_e32 v74, v28, v28
	s_waitcnt lgkmcnt(3)
	v_fma_f32 v27, v8, v98, -v142
	v_fma_f32 v26, v9, v96, -v143
	v_fmac_f32_e32 v89, v27, v27
	v_fmac_f32_e32 v87, v26, v26
	s_waitcnt lgkmcnt(2)
	v_fma_f32 v9, v10, v103, -v144
	v_fma_f32 v8, v11, v100, -v145
	v_fmac_f32_e32 v84, v9, v9
	v_fmac_f32_e32 v79, v8, v8
	s_waitcnt lgkmcnt(1)
	v_fma_f32 v7, v12, v97, -v146
	v_fma_f32 v6, v13, v94, -v147
	v_fmac_f32_e32 v81, v7, v7
	v_fmac_f32_e32 v75, v6, v6
	s_waitcnt lgkmcnt(0)
	v_fma_f32 v5, v14, v93, -v148
	v_fma_f32 v4, v15, v92, -v149
	v_lshl_add_u64 v[14:15], s[48:49], 0, v[162:163]
	flat_load_dword v10, v[14:15]
	flat_load_dword v11, v[14:15] offset:128
	flat_load_dword v12, v[14:15] offset:256
	flat_load_dword v13, v[14:15] offset:384
	v_and_b32_e32 v15, 64, v189
	ds_read_b32 v2, v108 offset:15872
	v_xor_b32_e32 v14, 16, v189
	v_add_u32_e32 v15, 64, v15
	v_cmp_lt_i32_e32 vcc, v14, v15
	v_fmac_f32_e32 v77, v5, v5
	v_cndmask_b32_e32 v14, v189, v14, vcc
	v_lshlrev_b32_e32 v14, 2, v14
	s_waitcnt lgkmcnt(0)
	v_fma_f32 v3, v16, v91, -v2
	v_fmac_f32_e32 v64, v4, v4
	v_fmac_f32_e32 v88, v3, v3
	v_or_b32_e32 v2, 0x3f00, v107
	v_add_u32_e32 v2, v106, v2
	ds_read_b32 v2, v2
	v_lshlrev_b32_e32 v162, 1, v175
	s_waitcnt lgkmcnt(0)
	v_fma_f32 v2, v17, v90, -v2
	v_fmac_f32_e32 v85, v2, v2
	v_add_f32_dpp v86, v86, v86 quad_perm:[1,0,3,2] row_mask:0xf bank_mask:0xf bound_ctrl:1
	v_add_f32_dpp v82, v82, v82 quad_perm:[1,0,3,2] row_mask:0xf bank_mask:0xf bound_ctrl:1
	v_add_f32_dpp v83, v83, v83 quad_perm:[1,0,3,2] row_mask:0xf bank_mask:0xf bound_ctrl:1
	v_add_f32_dpp v78, v78, v78 quad_perm:[1,0,3,2] row_mask:0xf bank_mask:0xf bound_ctrl:1
	v_add_f32_dpp v80, v80, v80 quad_perm:[1,0,3,2] row_mask:0xf bank_mask:0xf bound_ctrl:1
	v_add_f32_dpp v74, v74, v74 quad_perm:[1,0,3,2] row_mask:0xf bank_mask:0xf bound_ctrl:1
	v_add_f32_dpp v89, v89, v89 quad_perm:[1,0,3,2] row_mask:0xf bank_mask:0xf bound_ctrl:1
	v_add_f32_dpp v87, v87, v87 quad_perm:[1,0,3,2] row_mask:0xf bank_mask:0xf bound_ctrl:1
	v_add_f32_dpp v84, v84, v84 quad_perm:[1,0,3,2] row_mask:0xf bank_mask:0xf bound_ctrl:1
	v_add_f32_dpp v79, v79, v79 quad_perm:[1,0,3,2] row_mask:0xf bank_mask:0xf bound_ctrl:1
	v_add_f32_dpp v81, v81, v81 quad_perm:[1,0,3,2] row_mask:0xf bank_mask:0xf bound_ctrl:1
	v_add_f32_dpp v75, v75, v75 quad_perm:[1,0,3,2] row_mask:0xf bank_mask:0xf bound_ctrl:1
	v_add_f32_dpp v77, v77, v77 quad_perm:[1,0,3,2] row_mask:0xf bank_mask:0xf bound_ctrl:1
	v_add_f32_dpp v64, v64, v64 quad_perm:[1,0,3,2] row_mask:0xf bank_mask:0xf bound_ctrl:1
	v_add_f32_dpp v88, v88, v88 quad_perm:[1,0,3,2] row_mask:0xf bank_mask:0xf bound_ctrl:1
	v_add_f32_dpp v85, v85, v85 quad_perm:[1,0,3,2] row_mask:0xf bank_mask:0xf bound_ctrl:1
	v_add_f32_dpp v86, v86, v86 quad_perm:[2,3,0,1] row_mask:0xf bank_mask:0xf bound_ctrl:1
	v_add_f32_dpp v82, v82, v82 quad_perm:[2,3,0,1] row_mask:0xf bank_mask:0xf bound_ctrl:1
	v_add_f32_dpp v83, v83, v83 quad_perm:[2,3,0,1] row_mask:0xf bank_mask:0xf bound_ctrl:1
	v_add_f32_dpp v78, v78, v78 quad_perm:[2,3,0,1] row_mask:0xf bank_mask:0xf bound_ctrl:1
	v_add_f32_dpp v80, v80, v80 quad_perm:[2,3,0,1] row_mask:0xf bank_mask:0xf bound_ctrl:1
	v_add_f32_dpp v74, v74, v74 quad_perm:[2,3,0,1] row_mask:0xf bank_mask:0xf bound_ctrl:1
	v_add_f32_dpp v89, v89, v89 quad_perm:[2,3,0,1] row_mask:0xf bank_mask:0xf bound_ctrl:1
	v_add_f32_dpp v87, v87, v87 quad_perm:[2,3,0,1] row_mask:0xf bank_mask:0xf bound_ctrl:1
	v_add_f32_dpp v84, v84, v84 quad_perm:[2,3,0,1] row_mask:0xf bank_mask:0xf bound_ctrl:1
	v_add_f32_dpp v79, v79, v79 quad_perm:[2,3,0,1] row_mask:0xf bank_mask:0xf bound_ctrl:1
	v_add_f32_dpp v81, v81, v81 quad_perm:[2,3,0,1] row_mask:0xf bank_mask:0xf bound_ctrl:1
	v_add_f32_dpp v75, v75, v75 quad_perm:[2,3,0,1] row_mask:0xf bank_mask:0xf bound_ctrl:1
	v_add_f32_dpp v77, v77, v77 quad_perm:[2,3,0,1] row_mask:0xf bank_mask:0xf bound_ctrl:1
	v_add_f32_dpp v64, v64, v64 quad_perm:[2,3,0,1] row_mask:0xf bank_mask:0xf bound_ctrl:1
	v_add_f32_dpp v88, v88, v88 quad_perm:[2,3,0,1] row_mask:0xf bank_mask:0xf bound_ctrl:1
	v_add_f32_dpp v85, v85, v85 quad_perm:[2,3,0,1] row_mask:0xf bank_mask:0xf bound_ctrl:1
	v_add_f32_dpp v86, v86, v86 row_half_mirror row_mask:0xf bank_mask:0xf bound_ctrl:1
	v_add_f32_dpp v82, v82, v82 row_half_mirror row_mask:0xf bank_mask:0xf bound_ctrl:1
	v_add_f32_dpp v83, v83, v83 row_half_mirror row_mask:0xf bank_mask:0xf bound_ctrl:1
	v_add_f32_dpp v78, v78, v78 row_half_mirror row_mask:0xf bank_mask:0xf bound_ctrl:1
	v_add_f32_dpp v80, v80, v80 row_half_mirror row_mask:0xf bank_mask:0xf bound_ctrl:1
	v_add_f32_dpp v74, v74, v74 row_half_mirror row_mask:0xf bank_mask:0xf bound_ctrl:1
	v_add_f32_dpp v89, v89, v89 row_half_mirror row_mask:0xf bank_mask:0xf bound_ctrl:1
	v_add_f32_dpp v87, v87, v87 row_half_mirror row_mask:0xf bank_mask:0xf bound_ctrl:1
	v_add_f32_dpp v84, v84, v84 row_half_mirror row_mask:0xf bank_mask:0xf bound_ctrl:1
	v_add_f32_dpp v79, v79, v79 row_half_mirror row_mask:0xf bank_mask:0xf bound_ctrl:1
	v_add_f32_dpp v81, v81, v81 row_half_mirror row_mask:0xf bank_mask:0xf bound_ctrl:1
	v_add_f32_dpp v75, v75, v75 row_half_mirror row_mask:0xf bank_mask:0xf bound_ctrl:1
	v_add_f32_dpp v77, v77, v77 row_half_mirror row_mask:0xf bank_mask:0xf bound_ctrl:1
	v_add_f32_dpp v64, v64, v64 row_half_mirror row_mask:0xf bank_mask:0xf bound_ctrl:1
	v_add_f32_dpp v88, v88, v88 row_half_mirror row_mask:0xf bank_mask:0xf bound_ctrl:1
	v_add_f32_dpp v85, v85, v85 row_half_mirror row_mask:0xf bank_mask:0xf bound_ctrl:1
	v_add_f32_dpp v86, v86, v86 row_mirror row_mask:0xf bank_mask:0xf bound_ctrl:1
	v_add_f32_dpp v82, v82, v82 row_mirror row_mask:0xf bank_mask:0xf bound_ctrl:1
	v_add_f32_dpp v83, v83, v83 row_mirror row_mask:0xf bank_mask:0xf bound_ctrl:1
	v_add_f32_dpp v78, v78, v78 row_mirror row_mask:0xf bank_mask:0xf bound_ctrl:1
	v_add_f32_dpp v80, v80, v80 row_mirror row_mask:0xf bank_mask:0xf bound_ctrl:1
	v_add_f32_dpp v74, v74, v74 row_mirror row_mask:0xf bank_mask:0xf bound_ctrl:1
	v_add_f32_dpp v89, v89, v89 row_mirror row_mask:0xf bank_mask:0xf bound_ctrl:1
	v_add_f32_dpp v87, v87, v87 row_mirror row_mask:0xf bank_mask:0xf bound_ctrl:1
	v_add_f32_dpp v84, v84, v84 row_mirror row_mask:0xf bank_mask:0xf bound_ctrl:1
	v_add_f32_dpp v79, v79, v79 row_mirror row_mask:0xf bank_mask:0xf bound_ctrl:1
	v_add_f32_dpp v81, v81, v81 row_mirror row_mask:0xf bank_mask:0xf bound_ctrl:1
	v_add_f32_dpp v75, v75, v75 row_mirror row_mask:0xf bank_mask:0xf bound_ctrl:1
	v_add_f32_dpp v77, v77, v77 row_mirror row_mask:0xf bank_mask:0xf bound_ctrl:1
	v_add_f32_dpp v64, v64, v64 row_mirror row_mask:0xf bank_mask:0xf bound_ctrl:1
	v_add_f32_dpp v88, v88, v88 row_mirror row_mask:0xf bank_mask:0xf bound_ctrl:1
	v_add_f32_dpp v85, v85, v85 row_mirror row_mask:0xf bank_mask:0xf bound_ctrl:1
	ds_bpermute_b32 v140, v14, v86
	ds_bpermute_b32 v141, v14, v82
	ds_bpermute_b32 v142, v14, v83
	ds_bpermute_b32 v143, v14, v78
	ds_bpermute_b32 v144, v14, v80
	ds_bpermute_b32 v145, v14, v74
	ds_bpermute_b32 v146, v14, v89
	ds_bpermute_b32 v147, v14, v87
	s_waitcnt lgkmcnt(0)
	v_add_f32_e32 v86, v86, v140
	v_add_f32_e32 v82, v82, v141
	v_add_f32_e32 v83, v83, v142
	v_add_f32_e32 v78, v78, v143
	v_add_f32_e32 v80, v80, v144
	v_add_f32_e32 v74, v74, v145
	v_add_f32_e32 v89, v89, v146
	v_add_f32_e32 v87, v87, v147
	v_fmamk_f32 v86, v86, 0x3c000000, v1
	v_fmamk_f32 v82, v82, 0x3c000000, v1
	v_fmamk_f32 v83, v83, 0x3c000000, v1
	v_fmamk_f32 v78, v78, 0x3c000000, v1
	v_fmamk_f32 v80, v80, 0x3c000000, v1
	v_fmamk_f32 v74, v74, 0x3c000000, v1
	v_fmamk_f32 v89, v89, 0x3c000000, v1
	v_fmamk_f32 v87, v87, 0x3c000000, v1
	v_rsq_f32_e32 v86, v86
	v_rsq_f32_e32 v82, v82
	v_rsq_f32_e32 v83, v83
	v_rsq_f32_e32 v78, v78
	v_rsq_f32_e32 v80, v80
	v_rsq_f32_e32 v74, v74
	v_rsq_f32_e32 v89, v89
	v_rsq_f32_e32 v87, v87
	ds_bpermute_b32 v140, v14, v84
	ds_bpermute_b32 v141, v14, v79
	ds_bpermute_b32 v142, v14, v81
	ds_bpermute_b32 v143, v14, v75
	ds_bpermute_b32 v144, v14, v77
	ds_bpermute_b32 v145, v14, v64
	ds_bpermute_b32 v146, v14, v88
	ds_bpermute_b32 v147, v14, v85
	s_waitcnt lgkmcnt(0)
	v_add_f32_e32 v84, v84, v140
	v_add_f32_e32 v79, v79, v141
	v_add_f32_e32 v81, v81, v142
	v_add_f32_e32 v75, v75, v143
	v_add_f32_e32 v77, v77, v144
	v_add_f32_e32 v64, v64, v145
	v_add_f32_e32 v88, v88, v146
	v_add_f32_e32 v85, v85, v147
	v_fmamk_f32 v84, v84, 0x3c000000, v1
	v_fmamk_f32 v79, v79, 0x3c000000, v1
	v_fmamk_f32 v81, v81, 0x3c000000, v1
	v_fmamk_f32 v75, v75, 0x3c000000, v1
	v_fmamk_f32 v77, v77, 0x3c000000, v1
	v_fmamk_f32 v64, v64, 0x3c000000, v1
	v_fmamk_f32 v88, v88, 0x3c000000, v1
	v_fmamk_f32 v85, v85, 0x3c000000, v1
	v_rsq_f32_e32 v84, v84
	v_rsq_f32_e32 v79, v79
	v_rsq_f32_e32 v81, v81
	v_rsq_f32_e32 v75, v75
	v_rsq_f32_e32 v77, v77
	v_rsq_f32_e32 v64, v64
	v_rsq_f32_e32 v88, v88
	v_rsq_f32_e32 v85, v85
	s_nop 0
	v_mov_b32_e32 v17, v163
	s_waitcnt vmcnt(0)
	v_mul_f32_e32 v10, v174, v10
	v_mul_f32_e32 v11, v174, v11
	v_mul_f32_e32 v12, v174, v12
	v_mul_f32_e32 v13, v174, v13
	v_mul_f32_e32 v31, v31, v83
	v_mul_f32_e32 v31, v13, v31
	v_add_u32_e32 v31, 0x8000, v31
	v_mul_f32_e32 v30, v30, v78
	v_mul_f32_e32 v30, v13, v30
	v_add_u32_e32 v30, 0x8000, v30
	v_mul_f32_e32 v29, v29, v80
	v_mul_f32_e32 v29, v13, v29
	v_add_u32_e32 v29, 0x8000, v29
	v_mul_f32_e32 v28, v28, v74
	v_mul_f32_e32 v28, v13, v28
	v_add_u32_e32 v28, 0x8000, v28
	v_mul_f32_e32 v9, v9, v84
	v_mul_f32_e32 v9, v13, v9
	v_add_u32_e32 v9, 0x8000, v9
	v_mul_f32_e32 v25, v25, v84
	v_mul_f32_e32 v25, v12, v25
	v_add_u32_e32 v25, 0x8000, v25
	v_mul_f32_e32 v8, v8, v79
	v_mul_f32_e32 v8, v13, v8
	v_add_u32_e32 v8, 0x8000, v8
	v_mul_f32_e32 v7, v7, v81
	v_mul_f32_e32 v7, v13, v7
	v_add_u32_e32 v7, 0x8000, v7
	v_mul_f32_e32 v6, v6, v75
	v_mul_f32_e32 v6, v13, v6
	v_add_u32_e32 v6, 0x8000, v6
	v_mul_f32_e32 v5, v5, v77
	v_mul_f32_e32 v5, v13, v5
	v_add_u32_e32 v5, 0x8000, v5
	v_mul_f32_e32 v4, v4, v64
	v_mul_f32_e32 v4, v13, v4
	v_add_u32_e32 v4, 0x8000, v4
	v_lshlrev_b32_e32 v16, 13, v176
	v_mul_f32_e32 v3, v3, v88
	v_mul_f32_e32 v3, v13, v3
	v_add_u32_e32 v3, 0x8000, v3
	v_lshl_add_u64 v[14:15], s[6:7], 0, v[164:165]
	v_lshl_add_u64 v[14:15], v[14:15], 0, v[162:163]
	v_lshl_add_u64 v[14:15], v[14:15], 0, v[16:17]
	v_mul_f32_e32 v16, v73, v86
	v_mul_f32_e32 v16, v10, v16
	v_add_u32_e32 v16, 0x8000, v16
	global_store_short_d16_hi v[14:15], v16, off
	v_mul_f32_e32 v16, v58, v86
	v_mul_f32_e32 v16, v11, v16
	v_add_u32_e32 v16, 0x8000, v16
	global_store_short_d16_hi v[14:15], v16, off offset:64
	v_mul_f32_e32 v16, v76, v86
	v_mul_f32_e32 v16, v12, v16
	v_add_u32_e32 v16, 0x8000, v16
	global_store_short_d16_hi v[14:15], v16, off offset:128
	v_mul_f32_e32 v16, v33, v86
	v_mul_f32_e32 v16, v13, v16
	v_add_u32_e32 v16, 0x8000, v16
	global_store_short_d16_hi v[14:15], v16, off offset:192
	v_mul_f32_e32 v16, v72, v82
	v_mul_f32_e32 v16, v10, v16
	v_add_u32_e32 v16, 0x8000, v16
	global_store_short_d16_hi v[14:15], v16, off offset:2048
	v_mul_f32_e32 v16, v35, v82
	v_mul_f32_e32 v16, v11, v16
	v_add_u32_e32 v16, 0x8000, v16
	global_store_short_d16_hi v[14:15], v16, off offset:2112
	v_mul_f32_e32 v16, v63, v82
	v_mul_f32_e32 v16, v12, v16
	v_add_u32_e32 v16, 0x8000, v16
	global_store_short_d16_hi v[14:15], v16, off offset:2176
	v_mul_f32_e32 v16, v32, v82
	v_mul_f32_e32 v16, v13, v16
	v_add_u32_e32 v16, 0x8000, v16
	global_store_short_d16_hi v[14:15], v16, off offset:2240
	v_mul_f32_e32 v16, v71, v83
	v_mul_f32_e32 v16, v10, v16
	v_add_u32_e32 v32, 0x8000, v16
	v_add_co_u32_e32 v16, vcc, s0, v14
	s_movk_i32 s0, 0x5000
	s_nop 0
	v_addc_co_u32_e32 v17, vcc, 0, v15, vcc
	global_store_short_d16_hi v[16:17], v31, off offset:192
	v_mul_f32_e32 v31, v70, v78
	v_mul_f32_e32 v31, v10, v31
	v_add_u32_e32 v31, 0x8000, v31
	global_store_short_d16_hi v[16:17], v32, off
	v_mul_f32_e32 v32, v59, v83
	global_store_short_d16_hi v[16:17], v31, off offset:2048
	v_mul_f32_e32 v31, v36, v78
	v_mul_f32_e32 v32, v11, v32
	v_mul_f32_e32 v31, v11, v31
	v_add_u32_e32 v32, 0x8000, v32
	v_add_u32_e32 v31, 0x8000, v31
	global_store_short_d16_hi v[16:17], v32, off offset:64
	v_mul_f32_e32 v32, v65, v83
	global_store_short_d16_hi v[16:17], v31, off offset:2112
	v_mul_f32_e32 v31, v62, v78
	v_mul_f32_e32 v32, v12, v32
	v_mul_f32_e32 v31, v12, v31
	v_add_u32_e32 v32, 0x8000, v32
	v_add_u32_e32 v31, 0x8000, v31
	global_store_short_d16_hi v[16:17], v32, off offset:128
	global_store_short_d16_hi v[16:17], v31, off offset:2176
	global_store_short_d16_hi v[16:17], v30, off offset:2240
	v_mul_f32_e32 v16, v69, v80
	v_mul_f32_e32 v16, v10, v16
	v_add_u32_e32 v32, 0x8000, v16
	v_add_co_u32_e32 v16, vcc, s83, v14
	v_mul_f32_e32 v2, v2, v85
	s_nop 0
	v_addc_co_u32_e32 v17, vcc, 0, v15, vcc
	global_store_short_d16_hi v[16:17], v29, off offset:192
	v_mul_f32_e32 v29, v67, v74
	v_add_co_u32_e32 v30, vcc, s0, v14
	v_mul_f32_e32 v29, v10, v29
	s_nop 0
	v_addc_co_u32_e32 v31, vcc, 0, v15, vcc
	v_add_u32_e32 v29, 0x8000, v29
	global_store_short_d16_hi v[30:31], v32, off offset:-4096
	v_mul_f32_e32 v32, v37, v80
	global_store_short_d16_hi v[16:17], v29, off offset:2048
	v_mul_f32_e32 v29, v34, v74
	v_mul_f32_e32 v32, v11, v32
	v_mul_f32_e32 v29, v11, v29
	v_add_u32_e32 v32, 0x8000, v32
	v_add_u32_e32 v29, 0x8000, v29
	global_store_short_d16_hi v[16:17], v32, off offset:64
	v_mul_f32_e32 v32, v49, v80
	global_store_short_d16_hi v[16:17], v29, off offset:2112
	v_mul_f32_e32 v29, v48, v74
	v_mul_f32_e32 v32, v12, v32
	v_mul_f32_e32 v29, v12, v29
	v_add_u32_e32 v32, 0x8000, v32
	v_add_u32_e32 v29, 0x8000, v29
	global_store_short_d16_hi v[16:17], v32, off offset:128
	global_store_short_d16_hi v[16:17], v29, off offset:2176
	global_store_short_d16_hi v[16:17], v28, off offset:2240
	v_mul_f32_e32 v16, v68, v89
	v_mul_f32_e32 v16, v10, v16
	v_add_u32_e32 v16, 0x8000, v16
	global_store_short_d16_hi v[30:31], v16, off
	v_mul_f32_e32 v16, v61, v89
	v_mul_f32_e32 v16, v11, v16
	v_add_u32_e32 v16, 0x8000, v16
	global_store_short_d16_hi v[30:31], v16, off offset:64
	v_mul_f32_e32 v16, v47, v89
	v_mul_f32_e32 v16, v12, v16
	v_add_u32_e32 v16, 0x8000, v16
	global_store_short_d16_hi v[30:31], v16, off offset:128
	v_mul_f32_e32 v16, v27, v89
	v_mul_f32_e32 v16, v13, v16
	v_add_u32_e32 v16, 0x8000, v16
	global_store_short_d16_hi v[30:31], v16, off offset:192
	v_mul_f32_e32 v16, v66, v87
	v_mul_f32_e32 v16, v10, v16
	v_add_u32_e32 v16, 0x8000, v16
	global_store_short_d16_hi v[30:31], v16, off offset:2048
	v_mul_f32_e32 v16, v60, v87
	v_mul_f32_e32 v16, v11, v16
	v_add_u32_e32 v16, 0x8000, v16
	global_store_short_d16_hi v[30:31], v16, off offset:2112
	v_mul_f32_e32 v16, v46, v87
	v_mul_f32_e32 v16, v12, v16
	v_add_u32_e32 v16, 0x8000, v16
	global_store_short_d16_hi v[30:31], v16, off offset:2176
	v_mul_f32_e32 v16, v26, v87
	v_mul_f32_e32 v16, v13, v16
	v_add_u32_e32 v16, 0x8000, v16
	global_store_short_d16_hi v[30:31], v16, off offset:2240
	v_mul_f32_e32 v16, v57, v84
	v_mul_f32_e32 v16, v10, v16
	v_add_u32_e32 v28, 0x8000, v16
	v_add_co_u32_e32 v16, vcc, s90, v14
	s_mov_b32 s0, 0x9000
	s_nop 0
	v_addc_co_u32_e32 v17, vcc, 0, v15, vcc
	v_add_co_u32_e32 v26, vcc, s0, v14
	global_store_short_d16_hi v[16:17], v9, off offset:192
	s_nop 0
	v_addc_co_u32_e32 v27, vcc, 0, v15, vcc
	v_mul_f32_e32 v9, v56, v79
	v_mul_f32_e32 v9, v10, v9
	global_store_short_d16_hi v[26:27], v7, off offset:192
	v_mul_f32_e32 v7, v54, v75
	v_add_u32_e32 v9, 0x8000, v9
	global_store_short_d16_hi v[16:17], v8, off offset:2240
	v_mul_f32_e32 v8, v55, v81
	v_mul_f32_e32 v7, v10, v7
	global_store_short_d16_hi v[16:17], v9, off offset:2048
	v_mul_f32_e32 v9, v38, v79
	v_mul_f32_e32 v8, v10, v8
	v_add_u32_e32 v7, 0x8000, v7
	v_mul_f32_e32 v9, v11, v9
	v_add_u32_e32 v8, 0x8000, v8
	global_store_short_d16_hi v[26:27], v7, off offset:2048
	v_mul_f32_e32 v7, v40, v75
	v_add_u32_e32 v9, 0x8000, v9
	global_store_short_d16_hi v[26:27], v8, off
	v_mul_f32_e32 v8, v43, v81
	v_mul_f32_e32 v7, v11, v7
	global_store_short_d16_hi v[26:27], v28, off offset:-4096
	v_mul_f32_e32 v28, v41, v84
	global_store_short_d16_hi v[16:17], v9, off offset:2112
	v_mul_f32_e32 v9, v24, v79
	v_mul_f32_e32 v8, v11, v8
	v_add_u32_e32 v7, 0x8000, v7
	v_mul_f32_e32 v28, v11, v28
	v_mul_f32_e32 v9, v12, v9
	v_add_u32_e32 v8, 0x8000, v8
	global_store_short_d16_hi v[26:27], v7, off offset:2112
	v_mul_f32_e32 v7, v22, v75
	global_store_short_d16_hi v[26:27], v6, off offset:2240
	v_mul_f32_e32 v6, v53, v77
	v_add_u32_e32 v28, 0x8000, v28
	v_add_u32_e32 v9, 0x8000, v9
	global_store_short_d16_hi v[26:27], v8, off offset:64
	v_mul_f32_e32 v8, v23, v81
	v_mul_f32_e32 v7, v12, v7
	v_mul_f32_e32 v6, v10, v6
	global_store_short_d16_hi v[16:17], v28, off offset:64
	global_store_short_d16_hi v[16:17], v25, off offset:128
	global_store_short_d16_hi v[16:17], v9, off offset:2176
	v_mul_f32_e32 v8, v12, v8
	v_add_u32_e32 v7, 0x8000, v7
	v_add_u32_e32 v16, 0x8000, v6
	v_add_co_u32_e32 v6, vcc, s16, v14
	v_add_u32_e32 v8, 0x8000, v8
	global_store_short_d16_hi v[26:27], v7, off offset:2176
	v_addc_co_u32_e32 v7, vcc, 0, v15, vcc
	s_mov_b32 s0, 0xd000
	global_store_short_d16_hi v[26:27], v8, off offset:128
	v_add_co_u32_e32 v8, vcc, s0, v14
	global_store_short_d16_hi v[6:7], v5, off offset:192
	s_nop 0
	v_addc_co_u32_e32 v9, vcc, 0, v15, vcc
	v_mul_f32_e32 v5, v51, v64
	global_store_short_d16_hi v[6:7], v4, off offset:2240
	v_mul_f32_e32 v4, v52, v88
	global_store_short_d16_hi v[8:9], v3, off offset:192
	v_mul_f32_e32 v3, v50, v85
	v_mul_f32_e32 v5, v10, v5
	v_mul_f32_e32 v4, v10, v4
	v_mul_f32_e32 v3, v10, v3
	v_add_u32_e32 v5, 0x8000, v5
	v_add_u32_e32 v4, 0x8000, v4
	v_add_u32_e32 v3, 0x8000, v3
	v_mul_f32_e32 v14, v42, v77
	global_store_short_d16_hi v[6:7], v5, off offset:2048
	v_mul_f32_e32 v5, v39, v64
	global_store_short_d16_hi v[8:9], v4, off
	v_mul_f32_e32 v4, v45, v88
	global_store_short_d16_hi v[8:9], v3, off offset:2048
	v_mul_f32_e32 v3, v44, v85
	v_mul_f32_e32 v14, v11, v14
	v_mul_f32_e32 v5, v11, v5
	v_mul_f32_e32 v4, v11, v4
	v_mul_f32_e32 v3, v11, v3
	v_add_u32_e32 v14, 0x8000, v14
	v_add_u32_e32 v5, 0x8000, v5
	v_add_u32_e32 v4, 0x8000, v4
	v_add_u32_e32 v3, 0x8000, v3
	global_store_short_d16_hi v[6:7], v14, off offset:64
	v_mul_f32_e32 v14, v21, v77
	global_store_short_d16_hi v[6:7], v5, off offset:2112
	v_mul_f32_e32 v5, v20, v64
	global_store_short_d16_hi v[8:9], v4, off offset:64
	v_mul_f32_e32 v4, v19, v88
	global_store_short_d16_hi v[8:9], v3, off offset:2112
	v_mul_f32_e32 v3, v18, v85
	v_mul_f32_e32 v14, v12, v14
	v_mul_f32_e32 v5, v12, v5
	v_mul_f32_e32 v4, v12, v4
	v_mul_f32_e32 v3, v12, v3
	v_mul_f32_e32 v2, v13, v2
	v_add_u32_e32 v14, 0x8000, v14
	v_add_u32_e32 v5, 0x8000, v5
	v_add_u32_e32 v4, 0x8000, v4
	v_add_u32_e32 v3, 0x8000, v3
	v_add_u32_e32 v2, 0x8000, v2
	global_store_short_d16_hi v[8:9], v16, off offset:-4096
	global_store_short_d16_hi v[6:7], v14, off offset:128
	global_store_short_d16_hi v[6:7], v5, off offset:2176
	global_store_short_d16_hi v[8:9], v4, off offset:128
	global_store_short_d16_hi v[8:9], v3, off offset:2176
	global_store_short_d16_hi v[8:9], v2, off offset:2240
	s_branch .LBB0_1116
